# speedup vs baseline: 1.0240x; 1.0174x over previous
.LBB5_207:
	v_and_b32_e32 v6, 15, v0
	v_lshlrev_b32_e32 v73, 3, v6
	v_add_u32_e32 v76, 0x2800, v73
	s_waitcnt lgkmcnt(0)
	s_barrier
	v_mul_u32_u24_e32 v69, 0xe0, v81
	s_waitcnt vmcnt(12)
	ds_read2_b64 v[58:61], v76 offset0:32 offset1:48
	ds_read_b128 v[62:65], v69 offset:14080
	ds_read_b128 v[82:85], v69 offset:14096
	ds_read_b128 v[86:89], v69 offset:14112
	ds_read_b128 v[90:93], v69 offset:14128
	ds_read2_b64 v[94:97], v76 offset0:64 offset1:80
	v_and_b32_e32 v98, 24, v0
	v_add_u32_e32 v73, 0x3000, v73
	s_waitcnt lgkmcnt(4)
	v_mul_f32_e32 v0, v59, v63
	v_fmac_f32_e32 v0, v58, v62
	v_mul_f32_e32 v58, v61, v65
	s_waitcnt vmcnt(11)
	v_add_f32_e32 v0, v80, v0
	v_fmac_f32_e32 v58, v60, v64
	s_waitcnt lgkmcnt(0)
	v_mul_f32_e32 v62, v95, v83
	v_add_f32_e32 v0, v0, v58
	v_fmac_f32_e32 v62, v94, v82
	ds_read2_b64 v[58:61], v76 offset0:96 offset1:112
	v_add_f32_e32 v0, v0, v62
	v_mul_f32_e32 v62, v97, v85
	v_fmac_f32_e32 v62, v96, v84
	v_add_f32_e32 v0, v0, v62
	ds_read2_b64 v[62:65], v76 offset0:128 offset1:144
	s_waitcnt lgkmcnt(1)
	v_mul_f32_e32 v59, v59, v87
	v_fmac_f32_e32 v59, v58, v86
	v_mul_f32_e32 v58, v61, v89
	v_add_f32_e32 v0, v0, v59
	v_fmac_f32_e32 v58, v60, v88
	v_add_f32_e32 v0, v0, v58
	s_waitcnt lgkmcnt(0)
	v_mul_f32_e32 v58, v63, v91
	v_fmac_f32_e32 v58, v62, v90
	v_add_f32_e32 v0, v0, v58
	ds_read2_b64 v[58:61], v76 offset0:160 offset1:176
	ds_read_b128 v[80:83], v69 offset:14144
	v_mul_f32_e32 v62, v65, v93
	v_fmac_f32_e32 v62, v64, v92
	v_add_f32_e32 v0, v0, v62
	ds_read_b128 v[62:65], v69 offset:14160
	ds_read2_b64 v[84:87], v76 offset0:192 offset1:208
	s_waitcnt lgkmcnt(2)
	v_mul_f32_e32 v59, v59, v81
	v_fmac_f32_e32 v59, v58, v80
	v_mul_f32_e32 v58, v61, v83
	v_add_f32_e32 v0, v0, v59
	v_fmac_f32_e32 v58, v60, v82
	v_add_f32_e32 v0, v0, v58
	s_waitcnt lgkmcnt(0)
	v_mul_f32_e32 v58, v85, v63
	v_fmac_f32_e32 v58, v84, v62
	v_add_f32_e32 v0, v0, v58
	ds_read2_b64 v[58:61], v76 offset0:224 offset1:240
	ds_read_b128 v[80:83], v69 offset:14176
	v_mul_f32_e32 v62, v87, v65
	v_fmac_f32_e32 v62, v86, v64
	v_add_f32_e32 v0, v0, v62
	ds_read_b128 v[62:65], v69 offset:14192
	ds_read2_b64 v[84:87], v73 offset1:16
	s_waitcnt lgkmcnt(2)
	v_mul_f32_e32 v59, v59, v81
	v_fmac_f32_e32 v59, v58, v80
	v_mul_f32_e32 v58, v61, v83
	v_add_f32_e32 v0, v0, v59
	v_fmac_f32_e32 v58, v60, v82
	v_add_f32_e32 v0, v0, v58
	ds_read_b128 v[80:83], v69 offset:14224
	s_waitcnt lgkmcnt(1)
	v_mul_f32_e32 v58, v85, v63
	v_fmac_f32_e32 v58, v84, v62
	v_mul_f32_e32 v76, v87, v65
	v_add_f32_e32 v0, v0, v58
	ds_read_b128 v[58:61], v69 offset:14208
	v_fmac_f32_e32 v76, v86, v64
	ds_read2_b64 v[62:65], v73 offset0:32 offset1:48
	v_add_f32_e32 v0, v0, v76
	s_movk_i32 s4, 0x290
	s_waitcnt lgkmcnt(1)
	v_mov_b32_e32 v84, v59
	v_mov_b32_e32 v59, v61
	s_waitcnt lgkmcnt(0)
	v_pk_mov_b32 v[86:87], v[62:63], v[64:65] op_sel:[1,0]
	v_mov_b32_e32 v63, v65
	v_mov_b32_e32 v85, v60
	v_pk_mul_f32 v[58:59], v[62:63], v[58:59]
	s_waitcnt vmcnt(10)
	v_add_f32_e32 v54, v54, v55
	v_pk_fma_f32 v[62:63], v[86:87], v[84:85], v[58:59]
	ds_read2_b64 v[58:61], v73 offset0:64 offset1:80
	v_add_f32_e32 v0, v0, v62
	v_mov_b32_e32 v62, v81
	v_mov_b32_e32 v81, v83
	v_add_f32_e32 v0, v0, v63
	s_waitcnt lgkmcnt(0)
	v_pk_mov_b32 v[64:65], v[58:59], v[60:61] op_sel:[1,0]
	v_mov_b32_e32 v59, v61
	v_mov_b32_e32 v63, v82
	v_pk_mul_f32 v[58:59], v[58:59], v[80:81]
	v_add_f32_e32 v56, v56, v57
	v_pk_fma_f32 v[80:81], v[64:65], v[62:63], v[58:59]
	ds_read_b128 v[58:61], v69 offset:14240
	ds_read2_b64 v[62:65], v73 offset0:96 offset1:112
	v_add_f32_e32 v0, v0, v80
	v_add_f32_e32 v0, v0, v81
	ds_read_b128 v[80:83], v69 offset:14256
	s_waitcnt lgkmcnt(2)
	v_mov_b32_e32 v84, v59
	s_waitcnt lgkmcnt(1)
	v_pk_mov_b32 v[86:87], v[62:63], v[64:65] op_sel:[1,0]
	v_mov_b32_e32 v63, v65
	v_mov_b32_e32 v59, v61
	v_mov_b32_e32 v85, v60
	v_pk_mul_f32 v[58:59], v[62:63], v[58:59]
	s_nop 0
	v_pk_fma_f32 v[62:63], v[86:87], v[84:85], v[58:59]
	ds_read2_b64 v[58:61], v73 offset0:128 offset1:144
	v_add_f32_e32 v0, v0, v62
	s_waitcnt lgkmcnt(1)
	v_mov_b32_e32 v62, v81
	v_mov_b32_e32 v81, v83
	v_add_f32_e32 v0, v0, v63
	s_waitcnt lgkmcnt(0)
	v_pk_mov_b32 v[64:65], v[58:59], v[60:61] op_sel:[1,0]
	v_mov_b32_e32 v59, v61
	v_mov_b32_e32 v63, v82
	v_pk_mul_f32 v[58:59], v[58:59], v[80:81]
	s_nop 0
	v_pk_fma_f32 v[80:81], v[64:65], v[62:63], v[58:59]
	ds_read_b128 v[58:61], v69 offset:14272
	ds_read2_b64 v[62:65], v73 offset0:160 offset1:176
	v_add_f32_e32 v0, v0, v80
	v_add_f32_e32 v0, v0, v81
	ds_read_b128 v[80:83], v69 offset:14288
	s_waitcnt lgkmcnt(2)
	v_mov_b32_e32 v84, v59
	s_waitcnt lgkmcnt(1)
	v_pk_mov_b32 v[86:87], v[62:63], v[64:65] op_sel:[1,0]
	v_mov_b32_e32 v63, v65
	v_mov_b32_e32 v59, v61
	v_mov_b32_e32 v85, v60
	v_pk_mul_f32 v[58:59], v[62:63], v[58:59]
	s_nop 0
	v_pk_fma_f32 v[62:63], v[86:87], v[84:85], v[58:59]
	ds_read2_b64 v[58:61], v73 offset0:192 offset1:208
	v_add_f32_e32 v0, v0, v62
	s_waitcnt lgkmcnt(1)
	v_mov_b32_e32 v62, v81
	v_mov_b32_e32 v81, v83
	v_add_f32_e32 v0, v0, v63
	s_waitcnt lgkmcnt(0)
	v_pk_mov_b32 v[64:65], v[58:59], v[60:61] op_sel:[1,0]
	v_mov_b32_e32 v59, v61
	v_mov_b32_e32 v63, v82
	v_pk_mul_f32 v[58:59], v[58:59], v[80:81]
	s_nop 0
	v_pk_fma_f32 v[58:59], v[64:65], v[62:63], v[58:59]
	v_mad_u32_u24 v62, v6, s4, v79
	v_add_f32_e32 v0, v0, v58
	v_add_f32_e32 v61, v0, v59
	v_mbcnt_lo_u32_b32 v0, -1, 0
	v_mbcnt_hi_u32_b32 v58, -1, v0
	v_and_b32_e32 v6, 64, v58
	v_xor_b32_e32 v0, 8, v58
	v_add_u32_e32 v59, 64, v6
	v_cmp_lt_i32_e32 vcc, v0, v59
	ds_write_b32 v62, v61 offset:512
	s_nop 0
	v_cndmask_b32_e32 v0, v58, v0, vcc
	v_lshlrev_b32_e32 v6, 2, v0
	v_xor_b32_e32 v0, 16, v58
	v_cmp_lt_i32_e32 vcc, v0, v59
	s_nop 1
	v_add_f32_dpp v55, v54, v54 row_ror:8 row_mask:0xf bank_mask:0xf
	v_cndmask_b32_e32 v0, v58, v0, vcc
	v_lshlrev_b32_e32 v0, 2, v0
	v_add_f32_dpp v56, v56, v56 row_ror:8 row_mask:0xf bank_mask:0xf
	v_mov_b32_e32 v57, v55
	v_mov_b32_e32 v60, v56
	s_nop 1
	v_permlane16_swap_b32_e32 v57, v55
	v_permlane16_swap_b32_e32 v60, v56
	v_mul_u32_u24_e32 v54, 0x520, v78
	v_cmp_eq_u32_e32 vcc, 0, v98
	v_lshl_add_u32 v54, v66, 2, v54
	s_and_saveexec_b64 s[4:5], vcc
	s_cbranch_execz .LBB5_209
	v_add_f32_e32 v56, v56, v60
	v_add_f32_e32 v55, v55, v57
	v_mul_f32_e32 v55, 0x3e000000, v55
	v_mul_f32_e32 v56, 0x3e000000, v56
	ds_write2_b32 v54, v55, v56 offset1:164
.LBB5_209:
	s_or_b64 exec, exec, s[4:5]
	s_waitcnt vmcnt(9)
	v_add_f32_e32 v50, v50, v51
	v_add_f32_e32 v51, v52, v53
	s_nop 1
	v_add_f32_dpp v50, v50, v50 row_ror:8 row_mask:0xf bank_mask:0xf
	v_add_f32_dpp v51, v51, v51 row_ror:8 row_mask:0xf bank_mask:0xf
	v_mov_b32_e32 v52, v50
	v_mov_b32_e32 v53, v51
	s_nop 1
	v_permlane16_swap_b32_e32 v52, v50
	v_permlane16_swap_b32_e32 v53, v51
	s_and_saveexec_b64 s[4:5], vcc
	s_cbranch_execz .LBB5_211
	v_add_f32_e32 v51, v51, v53
	v_add_f32_e32 v50, v50, v52
	v_mul_f32_e32 v50, 0x3e000000, v50
	v_mul_f32_e32 v51, 0x3e000000, v51
	ds_write2_b32 v54, v50, v51 offset0:2 offset1:166
.LBB5_211:
	s_or_b64 exec, exec, s[4:5]
	s_waitcnt vmcnt(8)
	v_add_f32_e32 v46, v46, v47
	v_add_f32_e32 v47, v48, v49
	s_nop 1
	v_add_f32_dpp v46, v46, v46 row_ror:8 row_mask:0xf bank_mask:0xf
	v_add_f32_dpp v47, v47, v47 row_ror:8 row_mask:0xf bank_mask:0xf
	v_mov_b32_e32 v48, v46
	v_mov_b32_e32 v49, v47
	s_nop 1
	v_permlane16_swap_b32_e32 v48, v46
	v_permlane16_swap_b32_e32 v49, v47
	s_and_saveexec_b64 s[4:5], vcc
	s_cbranch_execz .LBB5_213
	v_add_f32_e32 v47, v47, v49
	v_add_f32_e32 v46, v46, v48
	v_mul_f32_e32 v46, 0x3e000000, v46
	v_mul_f32_e32 v47, 0x3e000000, v47
	ds_write2_b32 v54, v46, v47 offset0:4 offset1:168
.LBB5_213:
	s_or_b64 exec, exec, s[4:5]
	s_waitcnt vmcnt(7)
	v_add_f32_e32 v42, v42, v43
	v_add_f32_e32 v43, v44, v45
	s_nop 1
	v_add_f32_dpp v42, v42, v42 row_ror:8 row_mask:0xf bank_mask:0xf
	v_add_f32_dpp v43, v43, v43 row_ror:8 row_mask:0xf bank_mask:0xf
	v_mov_b32_e32 v44, v42
	v_mov_b32_e32 v45, v43
	s_nop 1
	v_permlane16_swap_b32_e32 v44, v42
	v_permlane16_swap_b32_e32 v45, v43
	s_and_saveexec_b64 s[4:5], vcc
	s_cbranch_execz .LBB5_215
	v_add_f32_e32 v43, v43, v45
	v_add_f32_e32 v42, v42, v44
	v_mul_f32_e32 v42, 0x3e000000, v42
	v_mul_f32_e32 v43, 0x3e000000, v43
	ds_write2_b32 v54, v42, v43 offset0:6 offset1:170
.LBB5_215:
	s_or_b64 exec, exec, s[4:5]
	s_waitcnt vmcnt(6)
	v_add_f32_e32 v34, v34, v35
	v_add_f32_e32 v35, v36, v37
	s_nop 1
	v_add_f32_dpp v34, v34, v34 row_ror:8 row_mask:0xf bank_mask:0xf
	v_add_f32_dpp v35, v35, v35 row_ror:8 row_mask:0xf bank_mask:0xf
	v_mov_b32_e32 v36, v34
	v_mov_b32_e32 v37, v35
	s_nop 1
	v_permlane16_swap_b32_e32 v36, v34
	v_permlane16_swap_b32_e32 v37, v35
	s_and_saveexec_b64 s[4:5], vcc
	s_cbranch_execz .LBB5_217
	v_add_f32_e32 v35, v35, v37
	v_add_f32_e32 v34, v34, v36
	v_mul_f32_e32 v34, 0x3e000000, v34
	v_mul_f32_e32 v35, 0x3e000000, v35
	ds_write2_b32 v54, v34, v35 offset0:8 offset1:172
.LBB5_217:
	s_or_b64 exec, exec, s[4:5]
	s_waitcnt vmcnt(5)
	v_add_f32_e32 v26, v26, v27
	v_add_f32_e32 v27, v28, v29
	s_nop 1
	v_add_f32_dpp v26, v26, v26 row_ror:8 row_mask:0xf bank_mask:0xf
	v_add_f32_dpp v27, v27, v27 row_ror:8 row_mask:0xf bank_mask:0xf
	v_mov_b32_e32 v28, v26
	v_mov_b32_e32 v29, v27
	s_nop 1
	v_permlane16_swap_b32_e32 v28, v26
	v_permlane16_swap_b32_e32 v29, v27
	s_and_saveexec_b64 s[4:5], vcc
	s_cbranch_execz .LBB5_219
	v_add_f32_e32 v27, v27, v29
	v_add_f32_e32 v26, v26, v28
	v_mul_f32_e32 v26, 0x3e000000, v26
	v_mul_f32_e32 v27, 0x3e000000, v27
	ds_write2_b32 v54, v26, v27 offset0:10 offset1:174
.LBB5_219:
	s_or_b64 exec, exec, s[4:5]
	s_waitcnt vmcnt(4)
	v_add_f32_e32 v26, v38, v39
	v_add_f32_e32 v27, v40, v41
	s_load_dwordx2 s[4:5], s[0:1], 0x50
	s_nop 1
	v_add_f32_dpp v26, v26, v26 row_ror:8 row_mask:0xf bank_mask:0xf
	v_add_f32_dpp v27, v27, v27 row_ror:8 row_mask:0xf bank_mask:0xf
	v_mov_b32_e32 v28, v26
	v_mov_b32_e32 v29, v27
	s_nop 1
	v_permlane16_swap_b32_e32 v28, v26
	v_permlane16_swap_b32_e32 v29, v27
	s_and_saveexec_b64 s[0:1], vcc
	s_cbranch_execz .LBB5_221
	v_add_f32_e32 v27, v27, v29
	v_add_f32_e32 v26, v26, v28
	v_mul_f32_e32 v26, 0x3e000000, v26
	v_mul_f32_e32 v27, 0x3e000000, v27
	ds_write2_b32 v54, v26, v27 offset0:12 offset1:176
.LBB5_221:
	s_or_b64 exec, exec, s[0:1]
	s_waitcnt vmcnt(3)
	v_add_f32_e32 v26, v30, v31
	v_add_f32_e32 v27, v32, v33
	s_nop 1
	v_add_f32_dpp v26, v26, v26 row_ror:8 row_mask:0xf bank_mask:0xf
	v_add_f32_dpp v27, v27, v27 row_ror:8 row_mask:0xf bank_mask:0xf
	v_mov_b32_e32 v28, v26
	v_mov_b32_e32 v29, v27
	s_nop 1
	v_permlane16_swap_b32_e32 v28, v26
	v_permlane16_swap_b32_e32 v29, v27
	s_and_saveexec_b64 s[0:1], vcc
	s_cbranch_execz .LBB5_223
	v_add_f32_e32 v27, v27, v29
	v_add_f32_e32 v26, v26, v28
	v_mul_f32_e32 v26, 0x3e000000, v26
	v_mul_f32_e32 v27, 0x3e000000, v27
	ds_write2_b32 v54, v26, v27 offset0:14 offset1:178
